# k_point: logical roles swapped (tid ^= 256) so the older hardware waves take role 1 (more post-gelu work: KV0 stores) on top of v22
# baseline (speedup 1.0000x reference)
_Z7k_pointPDF16_S_S_PKfS1_S1_S1_S1_S1_S1_S1_S1_S1_S1_S1_S1_S1_:
	v_xor_b32_e32 v0, 0x100, v0
	v_bfe_u32 v105, v0, 6, 2
	v_lshrrev_b32_e32 v104, 8, v0
	v_lshlrev_b32_e32 v1, 4, v105
	s_load_dwordx16 s[60:75], s[0:1], 0x0
	s_load_dwordx16 s[76:91], s[0:1], 0x40
	s_load_dwordx2 s[92:93], s[0:1], 0x80
	v_lshl_or_b32 v14, s2, 6, v1
	v_lshlrev_b32_e32 v107, 3, v104
	v_or_b32_e32 v2, v14, v107
	v_lshlrev_b32_e32 v2, 6, v2
	v_ashrrev_i32_e32 v3, 31, v2
	v_and_b32_e32 v103, 63, v0
	v_lshlrev_b64 v[2:3], 2, v[2:3]
	s_waitcnt lgkmcnt(0)
	v_lshl_add_u64 v[4:5], s[68:69], 0, v[2:3]
	v_lshlrev_b32_e32 v94, 4, v103
	v_mov_b32_e32 v95, 0
	v_lshl_add_u64 v[4:5], v[4:5], 0, v[94:95]
	v_lshl_add_u64 v[2:3], s[70:71], 0, v[2:3]
	v_mul_u32_u24_e32 v113, 0xe39, v0
	s_movk_i32 s2, 0xffee
	v_lshl_add_u64 v[2:3], v[2:3], 0, v[94:95]
	global_load_dwordx4 v[58:61], v[4:5], off nt
	global_load_dwordx4 v[50:53], v[4:5], off offset:1024 nt
	global_load_dwordx4 v[62:65], v[2:3], off nt
	global_load_dwordx4 v[54:57], v[2:3], off offset:1024 nt
	v_mul_i32_i24_sdwa v4, v113, s2 dst_sel:DWORD dst_unused:UNUSED_PAD src0_sel:WORD_1 src1_sel:DWORD
	s_movk_i32 s3, 0x48
	v_mul_u32_u24_sdwa v2, v113, s3 dst_sel:DWORD dst_unused:UNUSED_PAD src0_sel:WORD_1 src1_sel:DWORD
	v_add_lshl_u32 v96, v4, v0, 2
	v_lshlrev_b32_e32 v2, 2, v2
	v_mov_b32_e32 v3, v95
	v_ashrrev_i32_e32 v97, 31, v96
	v_lshl_add_u64 v[6:7], s[74:75], 0, v[2:3]
	v_lshlrev_b64 v[4:5], 2, v[96:97]
	v_or_b32_e32 v8, 0x200, v0
	v_lshl_add_u64 v[10:11], v[6:7], 0, v[4:5]
	v_mul_u32_u24_e32 v6, 0xe39, v8
	v_mul_i32_i24_sdwa v9, v6, s2 dst_sel:DWORD dst_unused:UNUSED_PAD src0_sel:WORD_1 src1_sel:DWORD
	v_mul_u32_u24_sdwa v6, v6, s3 dst_sel:DWORD dst_unused:UNUSED_PAD src0_sel:WORD_1 src1_sel:DWORD
	v_add_lshl_u32 v8, v9, v8, 2
	v_lshlrev_b32_e32 v6, 2, v6
	v_mov_b32_e32 v7, v95
	v_ashrrev_i32_e32 v9, 31, v8
	v_lshl_add_u64 v[12:13], s[74:75], 0, v[6:7]
	v_lshlrev_b64 v[8:9], 2, v[8:9]
	v_lshl_add_u64 v[12:13], v[12:13], 0, v[8:9]
	v_or_b32_e32 v106, 0x400, v0
	global_load_dwordx4 v[90:93], v[10:11], off
	global_load_dwordx4 v[86:89], v[12:13], off
	v_min_u32_e32 v12, 0x50f, v106
	v_mul_u32_u24_e32 v15, 0xe39, v12
	v_mul_i32_i24_sdwa v13, v15, s2 dst_sel:DWORD dst_unused:UNUSED_PAD src0_sel:WORD_1 src1_sel:DWORD
	v_mul_u32_u24_sdwa v10, v15, s3 dst_sel:DWORD dst_unused:UNUSED_PAD src0_sel:WORD_1 src1_sel:DWORD
	v_add_lshl_u32 v12, v13, v12, 2
	v_lshlrev_b32_e32 v98, 2, v10
	v_mov_b32_e32 v99, v95
	v_ashrrev_i32_e32 v13, 31, v12
	v_lshl_add_u64 v[10:11], s[74:75], 0, v[98:99]
	v_lshlrev_b64 v[100:101], 2, v[12:13]
	v_lshl_add_u64 v[10:11], v[10:11], 0, v[100:101]
	s_movk_i32 s2, 0x42
	global_load_dwordx4 v[82:85], v[10:11], off
	v_lshl_add_u64 v[10:11], s[78:79], 0, v[2:3]
	v_min_u32_sdwa v3, v15, s2 dst_sel:DWORD dst_unused:UNUSED_PAD src0_sel:WORD_1 src1_sel:DWORD
	v_lshl_add_u64 v[10:11], v[10:11], 0, v[4:5]
	v_lshl_add_u64 v[12:13], s[78:79], 0, v[6:7]
	v_mul_u32_u24_e32 v3, 0x48, v3
	v_lshl_add_u64 v[12:13], v[12:13], 0, v[8:9]
	global_load_dwordx4 v[74:77], v[10:11], off
	global_load_dwordx4 v[78:81], v[12:13], off
	v_lshlrev_b32_e32 v10, 2, v3
	v_mov_b32_e32 v11, v95
	v_lshl_add_u64 v[10:11], s[78:79], 0, v[10:11]
	v_min_u32_e32 v3, 0x47, v0
	v_lshl_add_u64 v[10:11], v[10:11], 0, v[100:101]
	v_lshlrev_b32_e32 v3, 2, v3
	global_load_dwordx4 v[70:73], v[10:11], off
	global_load_dword v109, v3, s[76:77]
	global_load_dword v110, v3, s[80:81]
	global_load_dword v111, v3, s[84:85]
	global_load_dword v112, v3, s[90:91]
	s_movk_i32 s2, 0x100
	v_and_b32_e32 v102, 15, v0
	v_cmp_gt_u32_e32 vcc, s2, v0
	s_movk_i32 s2, 0xff
	v_or_b32_e32 v97, v14, v102
	v_cmp_lt_u32_e64 s[4:5], s2, v0
	s_and_saveexec_b64 s[2:3], s[4:5]
	s_xor_b64 s[6:7], exec, s[2:3]
	s_cbranch_execz .LBB0_2
	v_lshl_add_u32 v10, v97, 1, v97
	v_ashrrev_i32_e32 v11, 31, v10
	v_mov_b32_e32 v69, v95
	v_lshl_add_u64 v[10:11], v[10:11], 2, s[66:67]
	global_load_dwordx3 v[66:68], v[10:11], off nt
